# stack3 = stack2 + LN2 last-layer vectors hoisted to LDS once (no per-batch barriers)
# baseline (speedup 1.0000x reference)
.LBB0_2071:
	s_cmp_lt_i32 s86, 18
	s_cselect_b64 s[2:3], -1, 0
	s_and_b64 s[6:7], s[2:3], s[0:1]
	s_andn2_b64 vcc, exec, s[6:7]
	s_cbranch_vccnz .LBB0_2092
	s_add_u32 s8, s80, 0x6000
	s_addc_u32 s9, s81, 0
	s_add_u32 s10, s82, 0x6000
	s_addc_u32 s11, s83, 0
	s_add_u32 s17, s84, 0x1cb00000
	s_addc_u32 s24, s85, 0
	s_add_u32 s25, s84, 0x2e300000
	s_addc_u32 s26, s85, 0
	v_readlane_b32 s0, v255, 25
	v_readlane_b32 s1, v255, 26
	s_cmpk_lt_i32 s0, 0x1000
	s_cselect_b64 s[0:1], -1, 0
	v_cndmask_b32_e64 v1, 0, 1, s[0:1]
	v_cmp_ne_u32_e64 s[2:3], 1, v1
	v_mbcnt_hi_u32_b32 v1, -1, v217
	s_waitcnt vmcnt(0)
	v_and_b32_e32 v2, 64, v1
	s_movk_i32 s27, 0x1000
	s_lshl_b32 s28, s94, 4
	s_mov_b32 s13, 0
	s_mov_b32 s29, 0x146000
	s_mov_b64 s[14:15], 0x1000
	s_mov_b32 s16, 0x3fb504f3
	v_add_u32_e32 v114, 64, v2
	v_xor_b32_e32 v115, 1, v1
	v_xor_b32_e32 v116, 2, v1
	v_xor_b32_e32 v117, 4, v1
	v_xor_b32_e32 v118, 8, v1
	v_xor_b32_e32 v119, 16, v1
	v_xor_b32_e32 v120, 32, v1
	v_mov_b32_e32 v121, 0x3727c5ac
	s_mov_b32 s30, 0xf800000
	v_mov_b32_e32 v122, 0x260
	s_mov_b32 s31, 0
	s_mov_b32 s33, 0
	s_mov_b32 s98, 0
	s_mov_b32 s99, 0
.Lln2f_fill:
	s_mul_i32 s12, s98, 0x3000
	v_mov_b32_e32 v18, v0
	s_lshl_b64 s[0:1], s[12:13], 2
	s_waitcnt lgkmcnt(0)
	s_add_u32 s0, s84, s0
	v_lshlrev_b32_e32 v2, 2, v18
	v_ashrrev_i32_e32 v3, 31, v2
	s_addc_u32 s1, s85, s1
	v_lshlrev_b64 v[6:7], 2, v[2:3]
	v_lshl_add_u64 v[2:3], s[0:1], 0, v[6:7]
	v_add_co_u32_e32 v14, vcc, s29, v2
	v_lshl_add_u64 v[16:17], s[10:11], 0, v[6:7]
	s_nop 0
	v_addc_co_u32_e32 v15, vcc, 0, v3, vcc
	v_lshl_add_u64 v[2:3], s[8:9], 0, v[6:7]
	global_load_dwordx4 v[2:5], v[2:3], off
	s_nop 0
	global_load_dwordx4 v[6:9], v[16:17], off
	global_load_dwordx4 v[10:13], v[14:15], off
	v_lshl_add_u32 v14, v18, 4, s99
	s_waitcnt vmcnt(2)
	ds_write_b128 v14, v[2:5] offset:8192
	s_waitcnt vmcnt(1)
	ds_write_b128 v14, v[6:9] offset:16384
	s_waitcnt vmcnt(0)
	ds_write_b128 v14, v[10:13]
	s_add_i32 s98, s98, 1
	s_addk_i32 s99, 0x6000
	s_cmp_lg_u32 s98, 4
	s_cbranch_scc1 .Lln2f_fill
	s_waitcnt lgkmcnt(0)
	s_barrier
	s_branch .LBB0_2074

.LBB0_2074:
	s_mul_i32 s99, s33, 0x6000
	v_readlane_b32 s0, v255, 25
	s_nop 2
	s_and_b64 vcc, exec, s[2:3]
	s_mov_b32 s12, s0
	v_readlane_b32 s1, v255, 26
	s_cbranch_vccz .LBB0_2076
	s_branch .LBB0_2073

.LBB0_2076:
	s_add_i32 s0, s31, s12
	s_add_i32 s1, s92, s12
	s_cmpk_gt_i32 s1, 0xfff
	s_cselect_b64 s[20:21], -1, 0
	s_cmpk_lt_i32 s1, 0x1000
	s_cselect_b32 s1, s92, 0
	s_add_i32 s4, s0, s1
	s_ashr_i32 s1, s0, 31
	s_lshl_b64 s[22:23], s[0:1], 13
	s_add_u32 s0, s17, s22
	s_addc_u32 s1, s24, s23
	s_ashr_i32 s5, s4, 31
	s_lshl_b64 s[18:19], s[4:5], 13
	s_add_u32 s4, s17, s18
	v_mov_b32_e32 v50, v216
	s_addc_u32 s5, s24, s19
	s_add_u32 s34, s25, s22
	v_ashrrev_i32_e32 v51, 31, v50
	s_addc_u32 s35, s26, s23
	v_lshlrev_b64 v[6:7], 1, v[50:51]
	s_add_u32 s36, s25, s18
	v_lshl_add_u64 v[62:63], s[34:35], 0, v[6:7]
	s_addc_u32 s37, s26, s19
	v_add_co_u32_e32 v66, vcc, s27, v62
	v_lshl_add_u64 v[72:73], s[36:37], 0, v[6:7]
	s_nop 0
	v_addc_co_u32_e32 v67, vcc, 0, v63, vcc
	v_lshlrev_b64 v[52:53], 2, v[50:51]
	v_add_co_u32_e32 v86, vcc, s27, v72
	v_lshl_add_u64 v[2:3], s[0:1], 0, v[52:53]
	s_nop 0
	v_addc_co_u32_e32 v87, vcc, 0, v73, vcc
	v_lshl_add_u64 v[4:5], s[4:5], 0, v[52:53]
	global_load_dwordx4 v[54:57], v[2:3], off nt
	global_load_dwordx4 v[58:61], v[2:3], off offset:1024 nt
	global_load_dwordx4 v[68:71], v[4:5], off nt
	global_load_dwordx4 v[124:127], v[4:5], off offset:1024 nt
	global_load_dwordx4 v[42:45], v[2:3], off offset:2048 nt
	global_load_dwordx4 v[38:41], v[2:3], off offset:3072 nt
	global_load_dwordx4 v[46:49], v[4:5], off offset:2048 nt
	global_load_dwordx4 v[34:37], v[4:5], off offset:3072 nt
	global_load_dwordx2 v[132:133], v[62:63], off nt
	global_load_dwordx2 v[136:137], v[62:63], off offset:512 nt
	global_load_dwordx2 v[138:139], v[62:63], off offset:1024 nt
	global_load_dwordx2 v[108:109], v[62:63], off offset:1536 nt
	global_load_dwordx2 v[134:135], v[72:73], off nt
	global_load_dwordx2 v[140:141], v[72:73], off offset:512 nt
	global_load_dwordx2 v[142:143], v[72:73], off offset:1024 nt
	global_load_dwordx2 v[104:105], v[72:73], off offset:1536 nt
	v_add_co_u32_e32 v2, vcc, s27, v2
	v_lshl_add_u64 v[64:65], v[62:63], 0, s[14:15]
	s_nop 0
	v_addc_co_u32_e32 v3, vcc, 0, v3, vcc
	v_add_co_u32_e32 v74, vcc, s27, v4
	v_lshl_add_u64 v[78:79], v[72:73], 0, s[14:15]
	s_nop 0
	v_addc_co_u32_e32 v75, vcc, 0, v5, vcc
	global_load_dwordx2 v[144:145], v[64:65], off offset:512 nt
	global_load_dwordx2 v[146:147], v[64:65], off offset:1024 nt
	global_load_dwordx2 v[112:113], v[64:65], off offset:1536 nt
	global_load_dwordx2 v[100:101], v[64:65], off offset:2048 nt
	global_load_dwordx2 v[148:149], v[78:79], off offset:512 nt
	global_load_dwordx2 v[150:151], v[78:79], off offset:1024 nt
	global_load_dwordx2 v[110:111], v[78:79], off offset:1536 nt
	global_load_dwordx2 v[98:99], v[78:79], off offset:2048 nt
	global_load_dwordx4 v[30:33], v[2:3], off nt
	global_load_dwordx4 v[22:25], v[2:3], off offset:1024 nt
	global_load_dwordx4 v[26:29], v[74:75], off nt
	global_load_dwordx4 v[18:21], v[74:75], off offset:1024 nt
	global_load_dwordx4 v[10:13], v[2:3], off offset:2048 nt
	global_load_dwordx4 v[6:9], v[2:3], off offset:3072 nt
	global_load_dwordx4 v[14:17], v[74:75], off offset:2048 nt
	s_nop 0
	global_load_dwordx4 v[2:5], v[74:75], off offset:3072 nt
	global_load_dwordx2 v[106:107], v[62:63], off offset:2048 nt
	global_load_dwordx2 v[94:95], v[62:63], off offset:2560 nt
	global_load_dwordx2 v[88:89], v[62:63], off offset:3072 nt
	global_load_dwordx2 v[80:81], v[62:63], off offset:3584 nt
	s_nop 0
	global_load_dwordx2 v[62:63], v[66:67], off nt
	global_load_dwordx2 v[96:97], v[64:65], off offset:2560 nt
	global_load_dwordx2 v[90:91], v[64:65], off offset:3072 nt
	global_load_dwordx2 v[82:83], v[64:65], off offset:3584 nt
	global_load_dwordx2 v[102:103], v[72:73], off offset:2048 nt
	global_load_dwordx2 v[76:77], v[72:73], off offset:2560 nt
	global_load_dwordx2 v[84:85], v[72:73], off offset:3072 nt
	global_load_dwordx2 v[74:75], v[72:73], off offset:3584 nt
	s_nop 0
	global_load_dwordx2 v[64:65], v[86:87], off nt
	global_load_dwordx2 v[92:93], v[78:79], off offset:2560 nt
	s_nop 0
	global_load_dwordx2 v[86:87], v[78:79], off offset:3072 nt
	s_nop 0
	global_load_dwordx2 v[78:79], v[78:79], off offset:3584 nt
	v_lshl_add_u32 v123, v50, 2, s99
	ds_read_b128 v[128:131], v123
	s_waitcnt vmcnt(39)
	v_lshlrev_b32_e32 v66, 16, v132
	v_and_b32_e32 v67, 0xffff0000, v132
	s_waitcnt vmcnt(11)
	v_lshlrev_b32_e32 v72, 16, v62
	v_and_b32_e32 v73, 0xffff0000, v62
	v_pk_add_f32 v[66:67], v[66:67], v[72:73]
	v_lshlrev_b32_e32 v72, 16, v133
	v_and_b32_e32 v73, 0xffff0000, v133
	v_lshlrev_b32_e32 v62, 16, v63
	v_and_b32_e32 v63, 0xffff0000, v63
	v_pk_add_f32 v[62:63], v[72:73], v[62:63]
	v_lshlrev_b32_e32 v72, 16, v134
	v_and_b32_e32 v73, 0xffff0000, v134
	s_waitcnt vmcnt(3)
	v_lshlrev_b32_e32 v132, 16, v64
	v_and_b32_e32 v133, 0xffff0000, v64
	v_pk_add_f32 v[72:73], v[72:73], v[132:133]
	v_lshlrev_b32_e32 v132, 16, v135
	v_and_b32_e32 v133, 0xffff0000, v135
	v_lshlrev_b32_e32 v64, 16, v65
	v_and_b32_e32 v65, 0xffff0000, v65
	v_pk_add_f32 v[152:153], v[132:133], v[64:65]
	ds_read_b128 v[132:135], v123 offset:1024
	s_waitcnt lgkmcnt(1)
	v_pk_mul_f32 v[62:63], v[62:63], v[130:131]
	v_pk_mul_f32 v[66:67], v[66:67], v[128:129]
	v_pk_fma_f32 v[64:65], v[56:57], s[16:17], v[62:63] op_sel_hi:[1,0,1]
	v_pk_mul_f32 v[56:57], v[72:73], v[128:129]
	v_pk_fma_f32 v[66:67], v[54:55], s[16:17], v[66:67] op_sel_hi:[1,0,1]
	v_pk_mul_f32 v[54:55], v[152:153], v[130:131]
	v_pk_fma_f32 v[56:57], v[68:69], s[16:17], v[56:57] op_sel_hi:[1,0,1]
	v_lshlrev_b32_e32 v62, 16, v136
	v_and_b32_e32 v63, 0xffff0000, v136
	v_lshlrev_b32_e32 v68, 16, v144
	v_and_b32_e32 v69, 0xffff0000, v144
	v_pk_fma_f32 v[54:55], v[70:71], s[16:17], v[54:55] op_sel_hi:[1,0,1]
	v_pk_add_f32 v[62:63], v[62:63], v[68:69]
	v_lshlrev_b32_e32 v68, 16, v137
	v_and_b32_e32 v69, 0xffff0000, v137
	v_lshlrev_b32_e32 v70, 16, v145
	v_and_b32_e32 v71, 0xffff0000, v145
	v_pk_add_f32 v[68:69], v[68:69], v[70:71]
	v_lshlrev_b32_e32 v70, 16, v140
	v_and_b32_e32 v71, 0xffff0000, v140
	v_lshlrev_b32_e32 v72, 16, v148
	v_and_b32_e32 v73, 0xffff0000, v148
	v_pk_add_f32 v[70:71], v[70:71], v[72:73]
	v_lshlrev_b32_e32 v72, 16, v141
	v_and_b32_e32 v73, 0xffff0000, v141
	v_lshlrev_b32_e32 v128, 16, v149
	v_and_b32_e32 v129, 0xffff0000, v149
	v_pk_add_f32 v[128:129], v[72:73], v[128:129]
	s_waitcnt lgkmcnt(0)
	v_pk_mul_f32 v[72:73], v[62:63], v[132:133]
	v_pk_mul_f32 v[62:63], v[68:69], v[134:135]
	v_pk_fma_f32 v[72:73], v[58:59], s[16:17], v[72:73] op_sel_hi:[1,0,1]
	v_pk_fma_f32 v[62:63], v[60:61], s[16:17], v[62:63] op_sel_hi:[1,0,1]
	v_pk_mul_f32 v[60:61], v[70:71], v[132:133]
	v_mov_b32_e32 v68, v66
	v_mov_b32_e32 v69, v72
	v_mov_b32_e32 v70, v67
	v_mov_b32_e32 v71, v73
	v_pk_fma_f32 v[60:61], v[124:125], s[16:17], v[60:61] op_sel_hi:[1,0,1]
	v_pk_add_f32 v[68:69], v[68:69], v[70:71]
	v_mov_b32_e32 v70, v65
	v_mov_b32_e32 v71, v63
	v_mov_b32_e32 v124, v64
	v_mov_b32_e32 v125, v62
	v_pk_add_f32 v[70:71], v[70:71], v[124:125]
	v_pk_mul_f32 v[58:59], v[128:129], v[134:135]
	v_pk_add_f32 v[68:69], v[68:69], v[70:71]
	v_pk_fma_f32 v[58:59], v[126:127], s[16:17], v[58:59] op_sel_hi:[1,0,1]
	v_add_f32_e32 v68, 0, v68
	v_add_f32_e32 v132, v68, v69
	v_mov_b32_e32 v68, v56
	v_mov_b32_e32 v69, v60
	v_mov_b32_e32 v70, v57
	v_mov_b32_e32 v71, v61
	v_pk_add_f32 v[68:69], v[68:69], v[70:71]
	v_mov_b32_e32 v70, v54
	v_mov_b32_e32 v71, v58
	v_mov_b32_e32 v124, v55
	v_mov_b32_e32 v125, v59
	v_pk_add_f32 v[70:71], v[70:71], v[124:125]
	ds_read_b128 v[124:127], v123 offset:2048
	v_pk_add_f32 v[68:69], v[68:69], v[70:71]
	v_lshlrev_b32_e32 v70, 16, v146
	v_add_f32_e32 v68, 0, v68
	v_add_f32_e32 v134, v68, v69
	v_lshlrev_b32_e32 v68, 16, v138
	v_and_b32_e32 v69, 0xffff0000, v138
	v_and_b32_e32 v71, 0xffff0000, v146
	v_pk_add_f32 v[68:69], v[68:69], v[70:71]
	v_lshlrev_b32_e32 v70, 16, v139
	v_and_b32_e32 v71, 0xffff0000, v139
	v_lshlrev_b32_e32 v128, 16, v147
	v_and_b32_e32 v129, 0xffff0000, v147
	v_pk_add_f32 v[70:71], v[70:71], v[128:129]
	v_lshlrev_b32_e32 v128, 16, v142
	v_and_b32_e32 v129, 0xffff0000, v142
	v_lshlrev_b32_e32 v130, 16, v150
	v_and_b32_e32 v131, 0xffff0000, v150
	v_pk_add_f32 v[136:137], v[128:129], v[130:131]
	v_lshlrev_b32_e32 v128, 16, v143
	v_and_b32_e32 v129, 0xffff0000, v143
	v_lshlrev_b32_e32 v130, 16, v151
	v_and_b32_e32 v131, 0xffff0000, v151
	v_pk_add_f32 v[138:139], v[128:129], v[130:131]
	ds_read_b128 v[128:131], v123 offset:3072
	s_waitcnt lgkmcnt(1)
	v_pk_mul_f32 v[140:141], v[68:69], v[124:125]
	v_pk_mul_f32 v[68:69], v[70:71], v[126:127]
	v_pk_fma_f32 v[70:71], v[42:43], s[16:17], v[140:141] op_sel_hi:[1,0,1]
	v_pk_fma_f32 v[68:69], v[44:45], s[16:17], v[68:69] op_sel_hi:[1,0,1]
	v_pk_mul_f32 v[44:45], v[136:137], v[124:125]
	v_pk_mul_f32 v[42:43], v[138:139], v[126:127]
	v_pk_fma_f32 v[44:45], v[46:47], s[16:17], v[44:45] op_sel_hi:[1,0,1]
	v_pk_fma_f32 v[42:43], v[48:49], s[16:17], v[42:43] op_sel_hi:[1,0,1]
	v_mov_b32_e32 v46, v70
	v_mov_b32_e32 v47, v69
	v_pk_mov_b32 v[48:49], v[70:71], v[68:69] op_sel:[1,0]
	v_cmp_lt_i32_e32 vcc, v115, v114
	v_pk_add_f32 v[46:47], v[46:47], v[48:49]
	v_mov_b32_e32 v48, v44
	v_pk_add_f32 v[124:125], v[46:47], v[46:47] op_sel:[0,1] op_sel_hi:[1,0]
	v_pk_mov_b32 v[46:47], v[44:45], v[42:43] op_sel:[1,0]
	v_mov_b32_e32 v49, v43
	v_pk_add_f32 v[46:47], v[46:47], v[48:49]
	v_lshlrev_b32_e32 v48, 16, v112
	v_pk_add_f32 v[126:127], v[46:47], v[46:47] op_sel:[0,1] op_sel_hi:[1,0]
	v_lshlrev_b32_e32 v46, 16, v108
	v_and_b32_e32 v47, 0xffff0000, v108
	v_and_b32_e32 v49, 0xffff0000, v112
	v_pk_add_f32 v[46:47], v[46:47], v[48:49]
	v_lshlrev_b32_e32 v48, 16, v109
	v_and_b32_e32 v49, 0xffff0000, v109
	v_lshlrev_b32_e32 v108, 16, v113
	v_and_b32_e32 v109, 0xffff0000, v113
	v_pk_add_f32 v[48:49], v[48:49], v[108:109]
	v_lshlrev_b32_e32 v108, 16, v104
	v_and_b32_e32 v109, 0xffff0000, v104
	v_lshlrev_b32_e32 v112, 16, v110
	v_and_b32_e32 v113, 0xffff0000, v110
	v_lshlrev_b32_e32 v104, 16, v105
	v_and_b32_e32 v105, 0xffff0000, v105
	v_lshlrev_b32_e32 v110, 16, v111
	v_and_b32_e32 v111, 0xffff0000, v111
	v_pk_add_f32 v[108:109], v[108:109], v[112:113]
	v_pk_add_f32 v[104:105], v[104:105], v[110:111]
	s_waitcnt lgkmcnt(0)
	v_pk_mul_f32 v[46:47], v[46:47], v[128:129]
	v_pk_mul_f32 v[48:49], v[48:49], v[130:131]
	s_nop 0
	v_pk_fma_f32 v[40:41], v[40:41], s[16:17], v[48:49] op_sel_hi:[1,0,1]
	v_pk_fma_f32 v[48:49], v[38:39], s[16:17], v[46:47] op_sel_hi:[1,0,1]
	v_pk_mul_f32 v[38:39], v[108:109], v[128:129]
	v_pk_mul_f32 v[46:47], v[104:105], v[130:131]
	ds_read_b128 v[108:111], v123 offset:4096
	v_pk_fma_f32 v[36:37], v[36:37], s[16:17], v[46:47] op_sel_hi:[1,0,1]
	v_pk_fma_f32 v[34:35], v[34:35], s[16:17], v[38:39] op_sel_hi:[1,0,1]
	v_lshlrev_b32_e32 v38, 16, v106
	v_and_b32_e32 v39, 0xffff0000, v106
	v_lshlrev_b32_e32 v46, 16, v100
	v_and_b32_e32 v47, 0xffff0000, v100
	v_pk_add_f32 v[38:39], v[38:39], v[46:47]
	v_lshlrev_b32_e32 v46, 16, v107
	v_and_b32_e32 v47, 0xffff0000, v107
	v_lshlrev_b32_e32 v100, 16, v101
	v_and_b32_e32 v101, 0xffff0000, v101
	v_pk_add_f32 v[46:47], v[46:47], v[100:101]
	v_lshlrev_b32_e32 v100, 16, v102
	v_and_b32_e32 v101, 0xffff0000, v102
	v_lshlrev_b32_e32 v106, 16, v98
	v_and_b32_e32 v107, 0xffff0000, v98
	v_pk_add_f32 v[106:107], v[100:101], v[106:107]
	v_lshlrev_b32_e32 v100, 16, v103
	v_and_b32_e32 v101, 0xffff0000, v103
	v_lshlrev_b32_e32 v98, 16, v99
	v_and_b32_e32 v99, 0xffff0000, v99
	v_pk_add_f32 v[102:103], v[100:101], v[98:99]
	ds_read_b128 v[98:101], v123 offset:5120
	s_waitcnt lgkmcnt(1)
	v_pk_mul_f32 v[136:137], v[38:39], v[108:109]
	v_pk_mul_f32 v[38:39], v[46:47], v[110:111]
	v_pk_fma_f32 v[46:47], v[30:31], s[16:17], v[136:137] op_sel_hi:[1,0,1]
	v_pk_fma_f32 v[38:39], v[32:33], s[16:17], v[38:39] op_sel_hi:[1,0,1]
	v_add_f32_e32 v104, v48, v49
	v_add_f32_e32 v112, v41, v40
	v_pk_mul_f32 v[30:31], v[106:107], v[108:109]
	v_pk_mul_f32 v[32:33], v[102:103], v[110:111]
	v_mov_b32_e32 v133, v46
	v_mov_b32_e32 v125, v47
	v_mov_b32_e32 v105, v39
	v_mov_b32_e32 v113, v38
	v_pk_fma_f32 v[28:29], v[28:29], s[16:17], v[32:33] op_sel_hi:[1,0,1]
	v_pk_fma_f32 v[26:27], v[26:27], s[16:17], v[30:31] op_sel_hi:[1,0,1]
	v_pk_add_f32 v[30:31], v[132:133], v[124:125]
	v_pk_add_f32 v[32:33], v[104:105], v[112:113]
	v_add_f32_e32 v128, v34, v35
	v_add_f32_e32 v130, v36, v37
	v_pk_add_f32 v[30:31], v[30:31], v[32:33]
	v_mov_b32_e32 v135, v26
	v_mov_b32_e32 v127, v27
	v_mov_b32_e32 v129, v28
	v_mov_b32_e32 v131, v29
	v_pk_add_f32 v[102:103], v[30:31], v[30:31] op_sel:[0,1] op_sel_hi:[1,0]
	v_pk_add_f32 v[30:31], v[134:135], v[126:127]
	v_pk_add_f32 v[32:33], v[128:129], v[130:131]
	s_nop 0
	v_pk_add_f32 v[30:31], v[30:31], v[32:33]
	v_lshlrev_b32_e32 v32, 16, v96
	v_pk_add_f32 v[104:105], v[30:31], v[30:31] op_sel:[0,1] op_sel_hi:[1,0]
	v_lshlrev_b32_e32 v30, 16, v94
	v_and_b32_e32 v31, 0xffff0000, v94
	v_and_b32_e32 v33, 0xffff0000, v96
	v_pk_add_f32 v[30:31], v[30:31], v[32:33]
	v_lshlrev_b32_e32 v32, 16, v95
	v_and_b32_e32 v33, 0xffff0000, v95
	v_lshlrev_b32_e32 v94, 16, v97
	v_and_b32_e32 v95, 0xffff0000, v97
	v_pk_add_f32 v[32:33], v[32:33], v[94:95]
	v_lshlrev_b32_e32 v94, 16, v76
	v_and_b32_e32 v95, 0xffff0000, v76
	s_waitcnt vmcnt(2)
	v_lshlrev_b32_e32 v96, 16, v92
	v_and_b32_e32 v97, 0xffff0000, v92
	v_lshlrev_b32_e32 v76, 16, v77
	v_and_b32_e32 v77, 0xffff0000, v77
	v_lshlrev_b32_e32 v92, 16, v93
	v_and_b32_e32 v93, 0xffff0000, v93
	v_pk_add_f32 v[94:95], v[94:95], v[96:97]
	v_pk_add_f32 v[92:93], v[76:77], v[92:93]
	s_waitcnt lgkmcnt(0)
	v_pk_mul_f32 v[30:31], v[30:31], v[98:99]
	v_pk_mul_f32 v[32:33], v[32:33], v[100:101]
	v_pk_fma_f32 v[76:77], v[22:23], s[16:17], v[30:31] op_sel_hi:[1,0,1]
	v_pk_fma_f32 v[24:25], v[24:25], s[16:17], v[32:33] op_sel_hi:[1,0,1]
	v_pk_mul_f32 v[22:23], v[94:95], v[98:99]
	v_pk_mul_f32 v[30:31], v[92:93], v[100:101]
	v_pk_fma_f32 v[18:19], v[18:19], s[16:17], v[22:23] op_sel_hi:[1,0,1]
	v_pk_fma_f32 v[20:21], v[20:21], s[16:17], v[30:31] op_sel_hi:[1,0,1]
	v_mov_b32_e32 v22, v76
	v_mov_b32_e32 v23, v25
	v_pk_mov_b32 v[30:31], v[76:77], v[24:25] op_sel:[1,0]
	v_mov_b32_e32 v32, v18
	v_pk_add_f32 v[22:23], v[22:23], v[30:31]
	v_pk_mov_b32 v[30:31], v[18:19], v[20:21] op_sel:[1,0]
	v_mov_b32_e32 v33, v21
	v_pk_add_f32 v[30:31], v[30:31], v[32:33]
	ds_read_b128 v[92:95], v123 offset:6144
	v_pk_add_f32 v[96:97], v[30:31], v[30:31] op_sel:[0,1] op_sel_hi:[1,0]
	v_lshlrev_b32_e32 v30, 16, v88
	v_and_b32_e32 v31, 0xffff0000, v88
	v_lshlrev_b32_e32 v32, 16, v90
	v_and_b32_e32 v33, 0xffff0000, v90
	v_pk_add_f32 v[30:31], v[30:31], v[32:33]
	v_lshlrev_b32_e32 v32, 16, v89
	v_and_b32_e32 v33, 0xffff0000, v89
	v_lshlrev_b32_e32 v88, 16, v91
	v_and_b32_e32 v89, 0xffff0000, v91
	v_pk_add_f32 v[32:33], v[32:33], v[88:89]
	v_lshlrev_b32_e32 v88, 16, v84
	v_and_b32_e32 v89, 0xffff0000, v84
	s_waitcnt vmcnt(1)
	v_lshlrev_b32_e32 v90, 16, v86
	v_and_b32_e32 v91, 0xffff0000, v86
	v_lshlrev_b32_e32 v84, 16, v85
	v_and_b32_e32 v85, 0xffff0000, v85
	v_lshlrev_b32_e32 v86, 16, v87
	v_and_b32_e32 v87, 0xffff0000, v87
	v_pk_add_f32 v[88:89], v[88:89], v[90:91]
	v_pk_add_f32 v[90:91], v[84:85], v[86:87]
	ds_read_b128 v[84:87], v123 offset:7168
	s_waitcnt lgkmcnt(1)
	v_pk_mul_f32 v[98:99], v[30:31], v[92:93]
	v_pk_mul_f32 v[30:31], v[32:33], v[94:95]
	v_pk_fma_f32 v[32:33], v[10:11], s[16:17], v[98:99] op_sel_hi:[1,0,1]
	v_pk_fma_f32 v[30:31], v[12:13], s[16:17], v[30:31] op_sel_hi:[1,0,1]
	v_pk_mul_f32 v[12:13], v[88:89], v[92:93]
	v_pk_mul_f32 v[10:11], v[90:91], v[94:95]
	v_pk_fma_f32 v[12:13], v[14:15], s[16:17], v[12:13] op_sel_hi:[1,0,1]
	v_lshlrev_b32_e32 v14, 16, v80
	v_and_b32_e32 v15, 0xffff0000, v80
	v_lshlrev_b32_e32 v94, 16, v82
	v_and_b32_e32 v95, 0xffff0000, v82
	v_lshlrev_b32_e32 v80, 16, v81
	v_and_b32_e32 v81, 0xffff0000, v81
	v_lshlrev_b32_e32 v82, 16, v83
	v_and_b32_e32 v83, 0xffff0000, v83
	v_pk_add_f32 v[14:15], v[14:15], v[94:95]
	v_pk_add_f32 v[80:81], v[80:81], v[82:83]
	v_lshlrev_b32_e32 v82, 16, v74
	v_and_b32_e32 v83, 0xffff0000, v74
	s_waitcnt vmcnt(0)
	v_lshlrev_b32_e32 v94, 16, v78
	v_and_b32_e32 v95, 0xffff0000, v78
	v_lshlrev_b32_e32 v74, 16, v75
	v_and_b32_e32 v75, 0xffff0000, v75
	v_lshlrev_b32_e32 v78, 16, v79
	v_and_b32_e32 v79, 0xffff0000, v79
	v_pk_add_f32 v[78:79], v[74:75], v[78:79]
	s_waitcnt lgkmcnt(0)
	v_pk_mul_f32 v[74:75], v[14:15], v[84:85]
	v_pk_mul_f32 v[14:15], v[80:81], v[86:87]
	v_pk_add_f32 v[22:23], v[22:23], v[22:23] op_sel:[0,1] op_sel_hi:[1,0]
	v_pk_fma_f32 v[14:15], v[8:9], s[16:17], v[14:15] op_sel_hi:[1,0,1]
	v_pk_fma_f32 v[74:75], v[6:7], s[16:17], v[74:75] op_sel_hi:[1,0,1]
	v_pk_fma_f32 v[10:11], v[16:17], s[16:17], v[10:11] op_sel_hi:[1,0,1]
	v_add_f32_e32 v16, v32, v33
	v_add_f32_e32 v88, v31, v30
	v_mov_b32_e32 v103, v74
	v_mov_b32_e32 v23, v75
	v_mov_b32_e32 v17, v15
	v_mov_b32_e32 v89, v14
	v_pk_add_f32 v[6:7], v[102:103], v[22:23]
	v_pk_add_f32 v[8:9], v[16:17], v[88:89]
	v_pk_add_f32 v[82:83], v[82:83], v[94:95]
	v_pk_add_f32 v[6:7], v[6:7], v[8:9]
	v_pk_mul_f32 v[8:9], v[78:79], v[86:87]
	v_add_f32_e32 v80, v6, v7
	v_cndmask_b32_e32 v6, v1, v115, vcc
	v_lshlrev_b32_e32 v94, 2, v6
	ds_bpermute_b32 v81, v94, v80
	v_pk_mul_f32 v[6:7], v[82:83], v[84:85]
	v_cmp_lt_i32_e32 vcc, v116, v114
	v_pk_fma_f32 v[22:23], v[2:3], s[16:17], v[6:7] op_sel_hi:[1,0,1]
	v_pk_fma_f32 v[16:17], v[4:5], s[16:17], v[8:9] op_sel_hi:[1,0,1]
	v_cndmask_b32_e32 v2, v1, v116, vcc
	s_waitcnt lgkmcnt(0)
	v_add_f32_e32 v4, v80, v81
	v_lshlrev_b32_e32 v95, 2, v2
	ds_bpermute_b32 v5, v95, v4
	v_cmp_lt_i32_e32 vcc, v117, v114
	v_add_f32_e32 v90, v12, v13
	v_add_f32_e32 v92, v10, v11
	v_mov_b32_e32 v105, v22
	v_mov_b32_e32 v97, v23
	v_mov_b32_e32 v91, v16
	s_waitcnt lgkmcnt(0)
	v_add_f32_e32 v6, v4, v5
	v_cndmask_b32_e32 v4, v1, v117, vcc
	v_mov_b32_e32 v93, v17
	v_pk_add_f32 v[2:3], v[104:105], v[96:97]
	v_lshlrev_b32_e32 v96, 2, v4
	v_pk_add_f32 v[4:5], v[90:91], v[92:93]
	ds_bpermute_b32 v7, v96, v6
	v_pk_add_f32 v[2:3], v[2:3], v[4:5]
	v_cmp_lt_i32_e32 vcc, v118, v114
	v_add_f32_e32 v2, v2, v3
	ds_bpermute_b32 v4, v94, v2
	v_cndmask_b32_e32 v5, v1, v118, vcc
	s_waitcnt lgkmcnt(1)
	v_add_f32_e32 v3, v6, v7
	v_lshlrev_b32_e32 v92, 2, v5
	ds_bpermute_b32 v5, v92, v3
	s_waitcnt lgkmcnt(1)
	v_add_f32_e32 v2, v2, v4
	ds_bpermute_b32 v4, v95, v2
	v_cmp_lt_i32_e32 vcc, v119, v114
	s_waitcnt lgkmcnt(1)
	v_add_f32_e32 v3, v3, v5
	v_cndmask_b32_e32 v5, v1, v119, vcc
	s_waitcnt lgkmcnt(0)
	v_add_f32_e32 v2, v2, v4
	ds_bpermute_b32 v4, v96, v2
	v_lshlrev_b32_e32 v93, 2, v5
	ds_bpermute_b32 v5, v93, v3
	v_cmp_lt_i32_e32 vcc, v120, v114
	s_waitcnt lgkmcnt(1)
	v_add_f32_e32 v2, v2, v4
	ds_bpermute_b32 v4, v92, v2
	s_waitcnt lgkmcnt(1)
	v_add_f32_e32 v3, v3, v5
	v_cndmask_b32_e32 v5, v1, v120, vcc
	v_lshlrev_b32_e32 v97, 2, v5
	ds_bpermute_b32 v5, v97, v3
	s_waitcnt lgkmcnt(1)
	v_add_f32_e32 v2, v2, v4
	ds_bpermute_b32 v4, v93, v2
	s_waitcnt lgkmcnt(1)
	v_add_f32_e32 v98, v3, v5
	v_fmamk_f32 v67, v98, 0xba000000, v67
	s_waitcnt lgkmcnt(0)
	v_add_f32_e32 v2, v2, v4
	ds_bpermute_b32 v4, v97, v2
	v_fmamk_f32 v73, v98, 0xba000000, v73
	v_fmac_f32_e32 v66, 0xba000000, v98
	v_fmac_f32_e32 v72, 0xba000000, v98
	v_mov_b32_e32 v5, v73
	s_waitcnt lgkmcnt(0)
	v_add_f32_e32 v99, v2, v4
	v_mov_b32_e32 v4, v67
	v_fmac_f32_e32 v64, 0xba000000, v98
	v_fmac_f32_e32 v62, 0xba000000, v98
	v_mov_b32_e32 v2, v66
	v_mov_b32_e32 v3, v72
	v_pk_mul_f32 v[4:5], v[4:5], v[4:5]
	v_fmamk_f32 v65, v98, 0xba000000, v65
	v_pk_fma_f32 v[2:3], v[2:3], v[2:3], v[4:5]
	v_mov_b32_e32 v4, v64
	v_mov_b32_e32 v5, v62
	v_fmamk_f32 v83, v98, 0xba000000, v63
	v_pk_mul_f32 v[4:5], v[4:5], v[4:5]
	v_mov_b32_e32 v82, v65
	v_fmamk_f32 v78, v99, 0xba000000, v55
	v_fmamk_f32 v84, v99, 0xba000000, v57
	v_fmamk_f32 v79, v99, 0xba000000, v59
	v_fmac_f32_e32 v58, 0xba000000, v99
	v_fmamk_f32 v85, v99, 0xba000000, v61
	v_fmac_f32_e32 v60, 0xba000000, v99
	v_pk_fma_f32 v[4:5], v[82:83], v[82:83], v[4:5]
	v_fmac_f32_e32 v54, 0xba000000, v99
	v_fmac_f32_e32 v56, 0xba000000, v99
	v_pk_add_f32 v[2:3], v[2:3], v[4:5]
	v_mov_b32_e32 v57, v60
	v_pk_mul_f32 v[4:5], v[84:85], v[84:85]
	v_mov_b32_e32 v55, v58
	v_pk_mul_f32 v[6:7], v[78:79], v[78:79]
	v_pk_fma_f32 v[4:5], v[56:57], v[56:57], v[4:5]
	v_pk_fma_f32 v[6:7], v[54:55], v[54:55], v[6:7]
	v_fmamk_f32 v69, v98, 0xba000000, v69
	v_fmac_f32_e32 v68, 0xba000000, v98
	v_fmamk_f32 v71, v98, 0xba000000, v71
	v_fmac_f32_e32 v70, 0xba000000, v98
	v_pk_add_f32 v[4:5], v[4:5], v[6:7]
	v_pk_mul_f32 v[6:7], v[68:69], v[68:69]
	v_pk_mul_f32 v[8:9], v[70:71], v[70:71]
	v_fmamk_f32 v43, v99, 0xba000000, v43
	v_fmac_f32_e32 v42, 0xba000000, v99
	v_fmamk_f32 v45, v99, 0xba000000, v45
	v_fmac_f32_e32 v44, 0xba000000, v99
	v_pk_mov_b32 v[80:81], v[8:9], v[6:7] op_sel:[1,0]
	v_mov_b32_e32 v9, v7
	v_pk_add_f32 v[2:3], v[2:3], v[2:3] op_sel_hi:[0,1]
	v_pk_add_f32 v[6:7], v[8:9], v[80:81]
	v_pk_mul_f32 v[8:9], v[42:43], v[42:43]
	v_pk_mul_f32 v[80:81], v[44:45], v[44:45]
	v_fmac_f32_e32 v48, 0xba000000, v98
	v_pk_mov_b32 v[86:87], v[80:81], v[8:9] op_sel:[1,0]
	v_mov_b32_e32 v81, v9
	v_fmac_f32_e32 v40, 0xba000000, v98
	v_fmamk_f32 v49, v98, 0xba000000, v49
	v_mul_f32_e32 v2, v48, v48
	v_pk_add_f32 v[8:9], v[86:87], v[80:81]
	v_fmamk_f32 v41, v98, 0xba000000, v41
	v_fmac_f32_e32 v34, 0xba000000, v99
	v_pk_fma_f32 v[80:81], v[48:49], v[48:49], v[2:3] op_sel_hi:[1,1,0]
	v_mul_f32_e32 v2, v40, v40
	v_fmac_f32_e32 v36, 0xba000000, v99
	v_fmamk_f32 v35, v99, 0xba000000, v35
	v_pk_fma_f32 v[86:87], v[40:41], v[40:41], v[2:3] op_sel_hi:[1,1,0]
	v_mul_f32_e32 v2, v34, v34
	v_pk_add_f32 v[6:7], v[6:7], v[6:7] op_sel_hi:[0,1]
	v_fmamk_f32 v37, v99, 0xba000000, v37
	v_pk_fma_f32 v[88:89], v[34:35], v[34:35], v[2:3] op_sel_hi:[1,1,0]
	v_mul_f32_e32 v2, v36, v36
	v_fmamk_f32 v39, v98, 0xba000000, v39
	v_fmac_f32_e32 v38, 0xba000000, v98
	v_fmamk_f32 v47, v98, 0xba000000, v47
	v_fmac_f32_e32 v46, 0xba000000, v98
	v_pk_add_f32 v[4:5], v[4:5], v[4:5] op_sel_hi:[0,1]
	v_pk_add_f32 v[8:9], v[8:9], v[8:9] op_sel_hi:[0,1]
	v_pk_fma_f32 v[90:91], v[36:37], v[36:37], v[2:3] op_sel_hi:[1,1,0]
	v_fmamk_f32 v29, v99, 0xba000000, v29
	v_fmac_f32_e32 v28, 0xba000000, v99
	v_fmamk_f32 v27, v99, 0xba000000, v27
	v_fmac_f32_e32 v26, 0xba000000, v99
	v_mul_f32_e32 v80, v46, v46
	v_mul_f32_e32 v86, v47, v47
	v_mul_f32_e32 v2, v38, v38
	v_mul_f32_e32 v6, v39, v39
	v_pk_add_f32 v[80:81], v[80:81], v[86:87]
	v_pk_add_f32 v[2:3], v[6:7], v[2:3]
	v_mul_f32_e32 v88, v26, v26
	v_mul_f32_e32 v90, v27, v27
	v_mul_f32_e32 v8, v28, v28
	v_mul_f32_e32 v4, v29, v29
	v_pk_add_f32 v[2:3], v[80:81], v[2:3]
	v_pk_add_f32 v[6:7], v[88:89], v[90:91]
	v_pk_add_f32 v[4:5], v[8:9], v[4:5]
	v_fmamk_f32 v25, v98, 0xba000000, v25
	v_fmac_f32_e32 v24, 0xba000000, v98
	v_fmamk_f32 v77, v98, 0xba000000, v77
	v_fmac_f32_e32 v76, 0xba000000, v98
	v_pk_add_f32 v[2:3], v[2:3], v[2:3] op_sel_hi:[0,1]
	v_pk_add_f32 v[4:5], v[6:7], v[4:5]
	v_pk_mul_f32 v[6:7], v[24:25], v[24:25]
	v_pk_mul_f32 v[8:9], v[76:77], v[76:77]
	v_fmac_f32_e32 v32, 0xba000000, v98
	v_pk_mov_b32 v[80:81], v[8:9], v[6:7] op_sel:[1,0]
	v_mov_b32_e32 v9, v7
	v_fmac_f32_e32 v30, 0xba000000, v98
	v_fmamk_f32 v33, v98, 0xba000000, v33
	v_mul_f32_e32 v2, v32, v32
	v_pk_add_f32 v[6:7], v[8:9], v[80:81]
	v_fmamk_f32 v31, v98, 0xba000000, v31
	v_pk_fma_f32 v[86:87], v[32:33], v[32:33], v[2:3] op_sel_hi:[1,1,0]
	v_mul_f32_e32 v2, v30, v30
	v_pk_add_f32 v[6:7], v[6:7], v[6:7] op_sel_hi:[0,1]
	v_pk_fma_f32 v[88:89], v[30:31], v[30:31], v[2:3] op_sel_hi:[1,1,0]
	v_fmamk_f32 v15, v98, 0xba000000, v15
	v_fmac_f32_e32 v14, 0xba000000, v98
	v_fmamk_f32 v75, v98, 0xba000000, v75
	v_fmac_f32_e32 v74, 0xba000000, v98
	v_mul_f32_e32 v86, v74, v74
	v_mul_f32_e32 v88, v75, v75
	v_mul_f32_e32 v2, v14, v14
	v_mul_f32_e32 v6, v15, v15
	v_pk_add_f32 v[86:87], v[86:87], v[88:89]
	v_pk_add_f32 v[2:3], v[6:7], v[2:3]
	v_pk_add_f32 v[4:5], v[4:5], v[4:5] op_sel_hi:[0,1]
	v_pk_add_f32 v[2:3], v[86:87], v[2:3]
	v_fmamk_f32 v21, v99, 0xba000000, v21
	v_add_f32_e32 v4, v2, v3
	v_fmac_f32_e32 v20, 0xba000000, v99
	v_fmamk_f32 v19, v99, 0xba000000, v19
	v_fmac_f32_e32 v18, 0xba000000, v99
	ds_bpermute_b32 v6, v94, v4
	v_pk_mul_f32 v[8:9], v[20:21], v[20:21]
	v_pk_mul_f32 v[80:81], v[18:19], v[18:19]
	v_fmac_f32_e32 v12, 0xba000000, v99
	v_pk_mov_b32 v[2:3], v[80:81], v[8:9] op_sel:[1,0]
	v_mov_b32_e32 v81, v9
	v_pk_add_f32 v[2:3], v[2:3], v[80:81]
	v_fmac_f32_e32 v10, 0xba000000, v99
	v_pk_add_f32 v[2:3], v[2:3], v[2:3] op_sel_hi:[0,1]
	s_waitcnt lgkmcnt(0)
	v_add_f32_e32 v2, v4, v6
	ds_bpermute_b32 v4, v95, v2
	v_fmamk_f32 v13, v99, 0xba000000, v13
	v_fmamk_f32 v11, v99, 0xba000000, v11
	v_fmamk_f32 v17, v99, 0xba000000, v17
	v_fmac_f32_e32 v16, 0xba000000, v99
	s_waitcnt lgkmcnt(0)
	v_add_f32_e32 v4, v2, v4
	ds_bpermute_b32 v55, v96, v4
	v_mul_f32_e32 v2, v12, v12
	v_pk_fma_f32 v[6:7], v[12:13], v[12:13], v[2:3] op_sel_hi:[1,1,0]
	v_mul_f32_e32 v2, v10, v10
	v_pk_fma_f32 v[8:9], v[10:11], v[10:11], v[2:3] op_sel_hi:[1,1,0]
	s_waitcnt lgkmcnt(0)
	v_add_f32_e32 v2, v4, v55
	ds_bpermute_b32 v4, v92, v2
	v_fmamk_f32 v23, v99, 0xba000000, v23
	v_fmac_f32_e32 v22, 0xba000000, v99
	v_mul_f32_e32 v6, v22, v22
	v_mul_f32_e32 v8, v23, v23
	s_waitcnt lgkmcnt(0)
	v_add_f32_e32 v55, v2, v4
	v_mul_f32_e32 v2, v16, v16
	v_mul_f32_e32 v4, v17, v17
	v_pk_add_f32 v[6:7], v[6:7], v[8:9]
	v_pk_add_f32 v[2:3], v[2:3], v[4:5]
	ds_bpermute_b32 v57, v93, v55
	v_pk_add_f32 v[2:3], v[6:7], v[2:3]
	s_waitcnt lgkmcnt(0)
	v_add_f32_e32 v55, v55, v57
	v_add_f32_e32 v2, v2, v3
	ds_bpermute_b32 v5, v94, v2
	ds_bpermute_b32 v57, v97, v55
	s_waitcnt lgkmcnt(1)
	v_add_f32_e32 v2, v2, v5
	ds_bpermute_b32 v5, v95, v2
	s_waitcnt lgkmcnt(1)
	v_add_f32_e32 v3, v55, v57
	v_fmamk_f32 v3, v3, 0x3a000000, v121
	v_mul_f32_e32 v4, 0x4f800000, v3
	v_cmp_gt_f32_e32 vcc, s30, v3
	s_waitcnt lgkmcnt(0)
	v_add_f32_e32 v2, v2, v5
	ds_bpermute_b32 v5, v96, v2
	v_cndmask_b32_e32 v3, v3, v4, vcc
	v_sqrt_f32_e32 v4, v3
	s_waitcnt lgkmcnt(0)
	v_add_f32_e32 v2, v2, v5
	ds_bpermute_b32 v5, v92, v2
	v_add_u32_e32 v6, -1, v4
	v_fma_f32 v7, -v6, v4, v3
	v_cmp_ge_f32_e64 s[0:1], 0, v7
	v_add_u32_e32 v7, 1, v4
	s_waitcnt lgkmcnt(0)
	v_add_f32_e32 v2, v2, v5
	ds_bpermute_b32 v5, v93, v2
	v_cndmask_b32_e64 v6, v4, v6, s[0:1]
	v_fma_f32 v4, -v7, v4, v3
	v_cmp_lt_f32_e64 s[0:1], 0, v4
	s_waitcnt lgkmcnt(0)
	v_add_f32_e32 v2, v2, v5
	v_cndmask_b32_e64 v4, v6, v7, s[0:1]
	v_mul_f32_e32 v6, 0x37800000, v4
	ds_bpermute_b32 v5, v97, v2
	v_cndmask_b32_e32 v4, v4, v6, vcc
	v_cmp_class_f32_e32 vcc, v3, v122
	s_waitcnt lgkmcnt(0)
	v_add_f32_e32 v2, v2, v5
	v_cndmask_b32_e32 v3, v4, v3, vcc
	v_div_scale_f32 v4, s[0:1], v3, v3, 1.0
	v_rcp_f32_e32 v6, v4
	v_fmamk_f32 v2, v2, 0x3a000000, v121
	v_mul_f32_e32 v5, 0x4f800000, v2
	v_cmp_gt_f32_e64 s[0:1], s30, v2
	v_fma_f32 v7, -v4, v6, 1.0
	v_fmac_f32_e32 v6, v7, v6
	v_cndmask_b32_e64 v2, v2, v5, s[0:1]
	v_div_scale_f32 v7, vcc, 1.0, v3, 1.0
	v_sqrt_f32_e32 v5, v2
	v_mul_f32_e32 v8, v7, v6
	v_fma_f32 v9, -v4, v8, v7
	v_fmac_f32_e32 v8, v9, v6
	v_fma_f32 v4, -v4, v8, v7
	v_add_u32_e32 v7, -1, v5
	v_fma_f32 v9, -v7, v5, v2
	v_cmp_ge_f32_e64 s[4:5], 0, v9
	v_add_u32_e32 v9, 1, v5
	v_div_fmas_f32 v4, v4, v6, v8
	v_cndmask_b32_e64 v7, v5, v7, s[4:5]
	v_fma_f32 v5, -v9, v5, v2
	v_cmp_lt_f32_e64 s[4:5], 0, v5
	v_div_fixup_f32 v80, v4, v3, 1.0
	v_mov_b32_e32 v81, v80
	v_cndmask_b32_e64 v5, v7, v9, s[4:5]
	v_mul_f32_e32 v7, 0x37800000, v5
	v_cndmask_b32_e64 v5, v5, v7, s[0:1]
	v_cmp_class_f32_e64 s[0:1], v2, v122
	v_pk_mul_f32 v[86:87], v[66:67], v[80:81] op_sel_hi:[1,0]
	v_pk_mul_f32 v[64:65], v[64:65], v[80:81] op_sel_hi:[1,0]
	v_cndmask_b32_e64 v55, v5, v2, s[0:1]
	v_div_scale_f32 v2, s[0:1], v55, v55, 1.0
	v_rcp_f32_e32 v57, v2
	s_add_u32 s0, s66, s22
	s_addc_u32 s1, s67, s23
	v_lshl_add_u64 v[52:53], s[0:1], 0, v[52:53]
	v_fma_f32 v3, -v2, v57, 1.0
	v_fmac_f32_e32 v57, v3, v57
	v_div_scale_f32 v3, vcc, 1.0, v55, 1.0
	v_mul_f32_e32 v59, v3, v57
	v_fma_f32 v4, -v2, v59, v3
	v_fmac_f32_e32 v59, v4, v57
	v_fma_f32 v61, -v2, v59, v3
	ds_read_b128 v[2:5], v123 offset:8192
	ds_read_b128 v[6:9], v123 offset:16384
	v_div_fmas_f32 v57, v61, v57, v59
	s_mov_b64 s[0:1], -1
	s_and_b64 vcc, exec, s[20:21]
	s_waitcnt lgkmcnt(0)
	v_pk_fma_f32 v[66:67], v[4:5], v[64:65], v[8:9]
	v_pk_fma_f32 v[64:65], v[2:3], v[86:87], v[6:7]
	global_store_dwordx4 v[52:53], v[64:67], off
	s_nop 1
	v_pk_mul_f32 v[66:67], v[72:73], v[80:81]
	s_cbranch_vccz .LBB0_2078
	ds_read_b128 v[86:89], v123 offset:9216
	ds_read_b128 v[90:93], v123 offset:17408
	v_mov_b32_e32 v64, v80
	v_mov_b32_e32 v65, v80
	v_mov_b32_e32 v63, v83
	v_pk_mul_f32 v[64:65], v[62:63], v[64:65]
	s_waitcnt lgkmcnt(0)
	v_pk_fma_f32 v[86:87], v[66:67], v[86:87], v[90:91]
	v_pk_fma_f32 v[88:89], v[64:65], v[88:89], v[92:93]
	global_store_dwordx4 v[52:53], v[86:89], off offset:1024
	s_mov_b64 s[0:1], 0

	.amdhsa_kernel _Z6mk_fwd4Args
		.amdhsa_group_segment_fixed_size 0
		.amdhsa_private_segment_fixed_size 0
		.amdhsa_kernarg_size 464
		.amdhsa_user_sgpr_count 2
		.amdhsa_user_sgpr_dispatch_ptr 0
		.amdhsa_user_sgpr_queue_ptr 0
		.amdhsa_user_sgpr_kernarg_segment_ptr 1
		.amdhsa_user_sgpr_dispatch_id 0
		.amdhsa_user_sgpr_kernarg_preload_length 0
		.amdhsa_user_sgpr_kernarg_preload_offset 0
		.amdhsa_user_sgpr_private_segment_size 0
		.amdhsa_uses_dynamic_stack 0
		.amdhsa_enable_private_segment 0
		.amdhsa_system_sgpr_workgroup_id_x 1
		.amdhsa_system_sgpr_workgroup_id_y 0
		.amdhsa_system_sgpr_workgroup_id_z 0
		.amdhsa_system_sgpr_workgroup_info 0
		.amdhsa_system_vgpr_workitem_id 0
		.amdhsa_next_free_vgpr 256
		.amdhsa_next_free_sgpr 102
		.amdhsa_accum_offset 256
		.amdhsa_reserve_vcc 1
		.amdhsa_float_round_mode_32 0
		.amdhsa_float_round_mode_16_64 0
		.amdhsa_float_denorm_mode_32 3
		.amdhsa_float_denorm_mode_16_64 3
		.amdhsa_dx10_clamp 1
		.amdhsa_ieee_mode 1
		.amdhsa_fp16_overflow 0
		.amdhsa_tg_split 0
		.amdhsa_exception_fp_ieee_invalid_op 0
		.amdhsa_exception_fp_denorm_src 0
		.amdhsa_exception_fp_ieee_div_zero 0
		.amdhsa_exception_fp_ieee_overflow 0
		.amdhsa_exception_fp_ieee_underflow 0
		.amdhsa_exception_fp_ieee_inexact 0
		.amdhsa_exception_int_div_zero 0
	.end_amdhsa_kernel

amdhsa.kernels:
  - .agpr_count:     0
    .args:
      - .offset:         0
        .size:           208
        .value_kind:     by_value
      - .offset:         208
        .size:           4
        .value_kind:     hidden_block_count_x
      - .offset:         212
        .size:           4
        .value_kind:     hidden_block_count_y
      - .offset:         216
        .size:           4
        .value_kind:     hidden_block_count_z
      - .offset:         220
        .size:           2
        .value_kind:     hidden_group_size_x
      - .offset:         222
        .size:           2
        .value_kind:     hidden_group_size_y
      - .offset:         224
        .size:           2
        .value_kind:     hidden_group_size_z
      - .offset:         226
        .size:           2
        .value_kind:     hidden_remainder_x
      - .offset:         228
        .size:           2
        .value_kind:     hidden_remainder_y
      - .offset:         230
        .size:           2
        .value_kind:     hidden_remainder_z
      - .offset:         248
        .size:           8
        .value_kind:     hidden_global_offset_x
      - .offset:         256
        .size:           8
        .value_kind:     hidden_global_offset_y
      - .offset:         264
        .size:           8
        .value_kind:     hidden_global_offset_z
      - .offset:         272
        .size:           2
        .value_kind:     hidden_grid_dims
      - .offset:         328
        .size:           4
        .value_kind:     hidden_dynamic_lds_size
    .group_segment_fixed_size: 0
    .kernarg_segment_align: 8
    .kernarg_segment_size: 464
    .language:       OpenCL C
    .language_version:
      - 2
      - 0
    .max_flat_workgroup_size: 512
    .name:           _Z6mk_fwd4Args
    .private_segment_fixed_size: 0
    .sgpr_count:     108
    .sgpr_spill_count: 66
    .symbol:         _Z6mk_fwd4Args.kd
    .uniform_work_group_size: 1
    .uses_dynamic_stack: false
    .vgpr_count:     256
    .vgpr_spill_count: 0
    .wavefront_size: 64
